# baseline (speedup 1.0000x reference)
_Z11pam_combinePKDF16_PKfS2_S2_Pf:
	s_load_dwordx8 s[8:15], s[0:1], 0x0
	s_load_dwordx2 s[20:21], s[0:1], 0x20
	v_lshl_or_b32 v0, s2, 8, v0
	s_mov_b32 s4, 0x24924925
	s_mov_b32 s5, 0xaaaaab
	s_movk_i32 s6, 0xfe80
	s_movk_i32 s7, 0x5556
	s_movk_i32 s16, 0x180
	s_movk_i32 s17, 0x68
	v_mul_hi_u32 v1, v0, s4
	v_mad_i32_i24 v2, v1, -7, v0
	v_mul_hi_u32 v3, v1, s5
	v_mad_i32_i24 v4, v3, s6, v1
	v_lshlrev_b32_e32 v7, 4, v3
	v_mul_u32_u24_e32 v5, s7, v7
	v_lshrrev_b32_e32 v5, 16, v5
	v_add_u32_e32 v7, 15, v7
	v_mul_u32_u24_e32 v6, s7, v7
	v_lshrrev_b32_e32 v6, 16, v6
	v_sub_u32_e32 v6, v6, v5
	v_mad_u32_u24 v7, v5, s16, v4
	v_lshlrev_b32_e32 v10, 4, v2
	v_lshlrev_b32_e32 v8, 2, v7
	v_mad_u32_u24 v9, v7, s17, v10
	v_lshl_add_u32 v7, v5, 1, v5
	v_lshrrev_b32_e32 v7, 4, v7
	v_cmp_eq_u32_e32 vcc, v7, v3
	v_add_u32_e32 v7, 0x100, v3
	v_mul_u32_u24_e32 v94, 0xc8, v1
	v_cndmask_b32_e32 v7, v7, v5, vcc
	v_mad_u32_u24 v7, v7, s16, v4
	v_lshlrev_b32_e32 v11, 2, v7
	v_mad_u32_u24 v18, v7, s17, v10
	v_add_u32_e32 v12, 0x600, v8
	v_add_u32_e32 v19, 0x9c00, v9
	v_add_u32_e32 v13, 0xc00, v8
	v_add_u32_e32 v20, 0x13800, v9
	v_add_u32_e32 v14, 0x1200, v8
	v_add_u32_e32 v21, 0x1d400, v9
	v_add_u32_e32 v15, 0x1800, v8
	v_add_u32_e32 v22, 0x27000, v9
	v_add_u32_e32 v16, 0x1e00, v8
	v_add_u32_e32 v23, 0x30c00, v9
	v_mul_u32_u24_e32 v7, 0x600, v6
	v_add_u32_e32 v17, v7, v8
	v_mul_u32_u24_e32 v7, 0x9c00, v6
	v_add_u32_e32 v24, v7, v9
	v_lshl_add_u32 v94, v2, 5, v94
	v_cmp_gt_u32_e32 vcc, 6, v2
	s_nop 1
	v_cndmask_b32_e64 v7, 0, 8, vcc
	s_waitcnt lgkmcnt(0)
	s_load_dword s18, s[14:15], 0x0
	global_load_dword v25, v11, s[10:11]
	global_load_dword v26, v12, s[10:11]
	global_load_dword v27, v13, s[10:11]
	global_load_dword v28, v14, s[10:11]
	global_load_dword v29, v15, s[10:11]
	global_load_dword v30, v16, s[10:11]
	global_load_dword v31, v17, s[10:11]
	global_load_dwordx4 v[32:35], v18, s[8:9] nt
	global_load_dwordx4 v[36:39], v19, s[8:9] nt
	global_load_dwordx4 v[40:43], v20, s[8:9] nt
	global_load_dwordx4 v[44:47], v21, s[8:9] nt
	global_load_dwordx4 v[48:51], v22, s[8:9] nt
	global_load_dwordx4 v[52:55], v23, s[8:9] nt
	global_load_dwordx4 v[56:59], v24, s[8:9] nt
	global_load_dwordx2 v[60:61], v94, s[12:13]
	v_add_u32_e32 v8, v94, v7
	v_lshl_add_u32 v9, v7, 1, v94
	v_mad_u32_u24 v10, v7, 3, v94
	global_load_dwordx2 v[62:63], v8, s[12:13]
	global_load_dwordx2 v[64:65], v9, s[12:13]
	global_load_dwordx2 v[66:67], v10, s[12:13]
	s_nop 0
	v_cmp_eq_u32_e32 vcc, 6, v6
	v_mov_b32_e32 v69, 0xff61b1e6
	s_waitcnt vmcnt(11)
	v_cndmask_b32_e32 v7, v69, v31, vcc
	v_max3_f32 v8, v25, v26, v27
	v_max3_f32 v8, v8, v28, v29
	v_max3_f32 v8, v8, v30, v7
	v_max_f32_e32 v69, v69, v8
	v_sub_f32_e32 v68, v25, v69
	v_sub_f32_e32 v70, v26, v69
	v_sub_f32_e32 v72, v27, v69
	v_sub_f32_e32 v74, v28, v69
	v_sub_f32_e32 v76, v29, v69
	v_sub_f32_e32 v78, v30, v69
	v_sub_f32_e32 v80, v31, v69
	v_exp_f32_e32 v68, v68
	v_exp_f32_e32 v70, v70
	v_exp_f32_e32 v72, v72
	v_exp_f32_e32 v74, v74
	v_exp_f32_e32 v76, v76
	v_exp_f32_e32 v78, v78
	v_exp_f32_e32 v80, v80
	s_nop 0
	v_cndmask_b32_e32 v80, 0, v80, vcc
	v_add_f32_e32 v71, v68, v70
	v_add_f32_e32 v71, v71, v72
	v_add_f32_e32 v71, v71, v74
	v_add_f32_e32 v71, v71, v76
	v_add_f32_e32 v71, v71, v78
	v_add_f32_e32 v71, v71, v80
	v_div_scale_f32 v73, s[22:23], v71, v71, 1.0
	v_rcp_f32_e32 v75, v73
	s_nop 0
	v_fma_f32 v77, -v73, v75, 1.0
	v_fmac_f32_e32 v75, v77, v75
	v_div_scale_f32 v77, vcc, 1.0, v71, 1.0
	v_mul_f32_e32 v79, v77, v75
	v_fma_f32 v81, -v73, v79, v77
	v_fmac_f32_e32 v79, v81, v75
	v_fma_f32 v73, -v73, v79, v77
	s_nop 1
	v_div_fmas_f32 v73, v73, v75, v79
	v_div_fixup_f32 v82, v73, v71, 1.0
	s_waitcnt vmcnt(10)
	v_cvt_f32_f16_sdwa v93, v32 dst_sel:DWORD dst_unused:UNUSED_PAD src0_sel:WORD_1
	v_cvt_f32_f16_e32 v92, v32
	v_pk_fma_f32 v[84:85], v[68:69], v[92:93], 0 op_sel_hi:[0,1,0]
	v_cvt_f32_f16_sdwa v93, v33 dst_sel:DWORD dst_unused:UNUSED_PAD src0_sel:WORD_1
	v_cvt_f32_f16_e32 v92, v33
	v_pk_fma_f32 v[86:87], v[68:69], v[92:93], 0 op_sel_hi:[0,1,0]
	v_cvt_f32_f16_sdwa v93, v34 dst_sel:DWORD dst_unused:UNUSED_PAD src0_sel:WORD_1
	v_cvt_f32_f16_e32 v92, v34
	v_pk_fma_f32 v[88:89], v[68:69], v[92:93], 0 op_sel_hi:[0,1,0]
	v_cvt_f32_f16_sdwa v93, v35 dst_sel:DWORD dst_unused:UNUSED_PAD src0_sel:WORD_1
	v_cvt_f32_f16_e32 v92, v35
	v_pk_fma_f32 v[90:91], v[68:69], v[92:93], 0 op_sel_hi:[0,1,0]
	s_waitcnt vmcnt(9)
	v_cvt_f32_f16_sdwa v93, v36 dst_sel:DWORD dst_unused:UNUSED_PAD src0_sel:WORD_1
	v_cvt_f32_f16_e32 v92, v36
	v_pk_fma_f32 v[84:85], v[70:71], v[92:93], v[84:85] op_sel_hi:[0,1,1]
	v_cvt_f32_f16_sdwa v93, v37 dst_sel:DWORD dst_unused:UNUSED_PAD src0_sel:WORD_1
	v_cvt_f32_f16_e32 v92, v37
	v_pk_fma_f32 v[86:87], v[70:71], v[92:93], v[86:87] op_sel_hi:[0,1,1]
	v_cvt_f32_f16_sdwa v93, v38 dst_sel:DWORD dst_unused:UNUSED_PAD src0_sel:WORD_1
	v_cvt_f32_f16_e32 v92, v38
	v_pk_fma_f32 v[88:89], v[70:71], v[92:93], v[88:89] op_sel_hi:[0,1,1]
	v_cvt_f32_f16_sdwa v93, v39 dst_sel:DWORD dst_unused:UNUSED_PAD src0_sel:WORD_1
	v_cvt_f32_f16_e32 v92, v39
	v_pk_fma_f32 v[90:91], v[70:71], v[92:93], v[90:91] op_sel_hi:[0,1,1]
	s_waitcnt vmcnt(8)
	v_cvt_f32_f16_sdwa v93, v40 dst_sel:DWORD dst_unused:UNUSED_PAD src0_sel:WORD_1
	v_cvt_f32_f16_e32 v92, v40
	v_pk_fma_f32 v[84:85], v[72:73], v[92:93], v[84:85] op_sel_hi:[0,1,1]
	v_cvt_f32_f16_sdwa v93, v41 dst_sel:DWORD dst_unused:UNUSED_PAD src0_sel:WORD_1
	v_cvt_f32_f16_e32 v92, v41
	v_pk_fma_f32 v[86:87], v[72:73], v[92:93], v[86:87] op_sel_hi:[0,1,1]
	v_cvt_f32_f16_sdwa v93, v42 dst_sel:DWORD dst_unused:UNUSED_PAD src0_sel:WORD_1
	v_cvt_f32_f16_e32 v92, v42
	v_pk_fma_f32 v[88:89], v[72:73], v[92:93], v[88:89] op_sel_hi:[0,1,1]
	v_cvt_f32_f16_sdwa v93, v43 dst_sel:DWORD dst_unused:UNUSED_PAD src0_sel:WORD_1
	v_cvt_f32_f16_e32 v92, v43
	v_pk_fma_f32 v[90:91], v[72:73], v[92:93], v[90:91] op_sel_hi:[0,1,1]
	s_waitcnt vmcnt(7)
	v_cvt_f32_f16_sdwa v93, v44 dst_sel:DWORD dst_unused:UNUSED_PAD src0_sel:WORD_1
	v_cvt_f32_f16_e32 v92, v44
	v_pk_fma_f32 v[84:85], v[74:75], v[92:93], v[84:85] op_sel_hi:[0,1,1]
	v_cvt_f32_f16_sdwa v93, v45 dst_sel:DWORD dst_unused:UNUSED_PAD src0_sel:WORD_1
	v_cvt_f32_f16_e32 v92, v45
	v_pk_fma_f32 v[86:87], v[74:75], v[92:93], v[86:87] op_sel_hi:[0,1,1]
	v_cvt_f32_f16_sdwa v93, v46 dst_sel:DWORD dst_unused:UNUSED_PAD src0_sel:WORD_1
	v_cvt_f32_f16_e32 v92, v46
	v_pk_fma_f32 v[88:89], v[74:75], v[92:93], v[88:89] op_sel_hi:[0,1,1]
	v_cvt_f32_f16_sdwa v93, v47 dst_sel:DWORD dst_unused:UNUSED_PAD src0_sel:WORD_1
	v_cvt_f32_f16_e32 v92, v47
	v_pk_fma_f32 v[90:91], v[74:75], v[92:93], v[90:91] op_sel_hi:[0,1,1]
	s_waitcnt vmcnt(6)
	v_cvt_f32_f16_sdwa v93, v48 dst_sel:DWORD dst_unused:UNUSED_PAD src0_sel:WORD_1
	v_cvt_f32_f16_e32 v92, v48
	v_pk_fma_f32 v[84:85], v[76:77], v[92:93], v[84:85] op_sel_hi:[0,1,1]
	v_cvt_f32_f16_sdwa v93, v49 dst_sel:DWORD dst_unused:UNUSED_PAD src0_sel:WORD_1
	v_cvt_f32_f16_e32 v92, v49
	v_pk_fma_f32 v[86:87], v[76:77], v[92:93], v[86:87] op_sel_hi:[0,1,1]
	v_cvt_f32_f16_sdwa v93, v50 dst_sel:DWORD dst_unused:UNUSED_PAD src0_sel:WORD_1
	v_cvt_f32_f16_e32 v92, v50
	v_pk_fma_f32 v[88:89], v[76:77], v[92:93], v[88:89] op_sel_hi:[0,1,1]
	v_cvt_f32_f16_sdwa v93, v51 dst_sel:DWORD dst_unused:UNUSED_PAD src0_sel:WORD_1
	v_cvt_f32_f16_e32 v92, v51
	v_pk_fma_f32 v[90:91], v[76:77], v[92:93], v[90:91] op_sel_hi:[0,1,1]
	s_waitcnt vmcnt(5)
	v_cvt_f32_f16_sdwa v93, v52 dst_sel:DWORD dst_unused:UNUSED_PAD src0_sel:WORD_1
	v_cvt_f32_f16_e32 v92, v52
	v_pk_fma_f32 v[84:85], v[78:79], v[92:93], v[84:85] op_sel_hi:[0,1,1]
	v_cvt_f32_f16_sdwa v93, v53 dst_sel:DWORD dst_unused:UNUSED_PAD src0_sel:WORD_1
	v_cvt_f32_f16_e32 v92, v53
	v_pk_fma_f32 v[86:87], v[78:79], v[92:93], v[86:87] op_sel_hi:[0,1,1]
	v_cvt_f32_f16_sdwa v93, v54 dst_sel:DWORD dst_unused:UNUSED_PAD src0_sel:WORD_1
	v_cvt_f32_f16_e32 v92, v54
	v_pk_fma_f32 v[88:89], v[78:79], v[92:93], v[88:89] op_sel_hi:[0,1,1]
	v_cvt_f32_f16_sdwa v93, v55 dst_sel:DWORD dst_unused:UNUSED_PAD src0_sel:WORD_1
	v_cvt_f32_f16_e32 v92, v55
	v_pk_fma_f32 v[90:91], v[78:79], v[92:93], v[90:91] op_sel_hi:[0,1,1]
	s_waitcnt vmcnt(4)
	v_cvt_f32_f16_sdwa v93, v56 dst_sel:DWORD dst_unused:UNUSED_PAD src0_sel:WORD_1
	v_cvt_f32_f16_e32 v92, v56
	v_pk_fma_f32 v[84:85], v[80:81], v[92:93], v[84:85] op_sel_hi:[0,1,1]
	v_cvt_f32_f16_sdwa v93, v57 dst_sel:DWORD dst_unused:UNUSED_PAD src0_sel:WORD_1
	v_cvt_f32_f16_e32 v92, v57
	v_pk_fma_f32 v[86:87], v[80:81], v[92:93], v[86:87] op_sel_hi:[0,1,1]
	v_cvt_f32_f16_sdwa v93, v58 dst_sel:DWORD dst_unused:UNUSED_PAD src0_sel:WORD_1
	v_cvt_f32_f16_e32 v92, v58
	v_pk_fma_f32 v[88:89], v[80:81], v[92:93], v[88:89] op_sel_hi:[0,1,1]
	v_cvt_f32_f16_sdwa v93, v59 dst_sel:DWORD dst_unused:UNUSED_PAD src0_sel:WORD_1
	v_cvt_f32_f16_e32 v92, v59
	v_pk_fma_f32 v[90:91], v[80:81], v[92:93], v[90:91] op_sel_hi:[0,1,1]
	v_pk_mul_f32 v[84:85], v[82:83], v[84:85] op_sel_hi:[0,1]
	v_pk_mul_f32 v[86:87], v[82:83], v[86:87] op_sel_hi:[0,1]
	v_pk_mul_f32 v[88:89], v[82:83], v[88:89] op_sel_hi:[0,1]
	v_pk_mul_f32 v[90:91], v[82:83], v[90:91] op_sel_hi:[0,1]
	s_waitcnt vmcnt(0) lgkmcnt(0)
	s_mov_b32 s19, s18
	v_pk_fma_f32 v[84:85], s[18:19], v[84:85], v[60:61]
	v_pk_fma_f32 v[86:87], s[18:19], v[86:87], v[62:63]
	v_pk_fma_f32 v[88:89], s[18:19], v[88:89], v[64:65]
	v_pk_fma_f32 v[90:91], s[18:19], v[90:91], v[66:67]
	v_cmp_gt_u32_e32 vcc, 6, v2
	global_store_dwordx2 v94, v[84:85], s[20:21]
	s_and_b64 exec, exec, vcc
	global_store_dwordx4 v94, v[86:89], s[20:21] offset:8
	global_store_dwordx2 v94, v[90:91], s[20:21] offset:24
	s_endpgm

	.amdhsa_kernel _Z11pam_combinePKDF16_PKfS2_S2_Pf
		.amdhsa_group_segment_fixed_size 0
		.amdhsa_private_segment_fixed_size 0
		.amdhsa_kernarg_size 40
		.amdhsa_user_sgpr_count 2
		.amdhsa_user_sgpr_dispatch_ptr 0
		.amdhsa_user_sgpr_queue_ptr 0
		.amdhsa_user_sgpr_kernarg_segment_ptr 1
		.amdhsa_user_sgpr_dispatch_id 0
		.amdhsa_user_sgpr_kernarg_preload_length 0
		.amdhsa_user_sgpr_kernarg_preload_offset 0
		.amdhsa_user_sgpr_private_segment_size 0
		.amdhsa_uses_dynamic_stack 0
		.amdhsa_enable_private_segment 0
		.amdhsa_system_sgpr_workgroup_id_x 1
		.amdhsa_system_sgpr_workgroup_id_y 0
		.amdhsa_system_sgpr_workgroup_id_z 0
		.amdhsa_system_sgpr_workgroup_info 0
		.amdhsa_system_vgpr_workitem_id 0
		.amdhsa_next_free_vgpr 96
		.amdhsa_next_free_sgpr 32
		.amdhsa_accum_offset 96
		.amdhsa_reserve_vcc 1
		.amdhsa_float_round_mode_32 0
		.amdhsa_float_round_mode_16_64 0
		.amdhsa_float_denorm_mode_32 3
		.amdhsa_float_denorm_mode_16_64 3
		.amdhsa_dx10_clamp 1
		.amdhsa_ieee_mode 1
		.amdhsa_fp16_overflow 0
		.amdhsa_tg_split 0
		.amdhsa_exception_fp_ieee_invalid_op 0
		.amdhsa_exception_fp_denorm_src 0
		.amdhsa_exception_fp_ieee_div_zero 0
		.amdhsa_exception_fp_ieee_overflow 0
		.amdhsa_exception_fp_ieee_underflow 0
		.amdhsa_exception_fp_ieee_inexact 0
		.amdhsa_exception_int_div_zero 0
	.end_amdhsa_kernel

amdhsa.kernels:
  - .agpr_count:     0
    .args:
      - .actual_access:  read_only
        .address_space:  global
        .offset:         0
        .size:           8
        .value_kind:     global_buffer
      - .actual_access:  read_only
        .address_space:  global
        .offset:         8
        .size:           8
        .value_kind:     global_buffer
      - .actual_access:  read_only
        .address_space:  global
        .offset:         16
        .size:           8
        .value_kind:     global_buffer
      - .actual_access:  read_only
        .address_space:  global
        .offset:         24
        .size:           8
        .value_kind:     global_buffer
      - .actual_access:  write_only
        .address_space:  global
        .offset:         32
        .size:           8
        .value_kind:     global_buffer
      - .actual_access:  write_only
        .address_space:  global
        .offset:         40
        .size:           8
        .value_kind:     global_buffer
      - .actual_access:  write_only
        .address_space:  global
        .offset:         48
        .size:           8
        .value_kind:     global_buffer
      - .actual_access:  write_only
        .address_space:  global
        .offset:         56
        .size:           8
        .value_kind:     global_buffer
      - .actual_access:  write_only
        .address_space:  global
        .offset:         64
        .size:           8
        .value_kind:     global_buffer
    .group_segment_fixed_size: 29184
    .kernarg_segment_align: 8
    .kernarg_segment_size: 72
    .language:       OpenCL C
    .language_version:
      - 2
      - 0
    .max_flat_workgroup_size: 256
    .name:           _Z8pam_prepPKfS0_S0_S0_PDv4_jS2_S2_PfS3_
    .private_segment_fixed_size: 0
    .sgpr_count:     28
    .sgpr_spill_count: 0
    .symbol:         _Z8pam_prepPKfS0_S0_S0_PDv4_jS2_S2_PfS3_.kd
    .uniform_work_group_size: 1
    .uses_dynamic_stack: false
    .vgpr_count:     168
    .vgpr_spill_count: 0
    .wavefront_size: 64
  - .agpr_count:     0
    .args:
      - .address_space:  global
        .offset:         0
        .size:           8
        .value_kind:     global_buffer
      - .actual_access:  read_only
        .address_space:  global
        .offset:         8
        .size:           8
        .value_kind:     global_buffer
      - .address_space:  global
        .offset:         16
        .size:           8
        .value_kind:     global_buffer
      - .actual_access:  read_only
        .address_space:  global
        .offset:         24
        .size:           8
        .value_kind:     global_buffer
      - .actual_access:  read_only
        .address_space:  global
        .offset:         32
        .size:           8
        .value_kind:     global_buffer
      - .actual_access:  write_only
        .address_space:  global
        .offset:         40
        .size:           8
        .value_kind:     global_buffer
      - .actual_access:  write_only
        .address_space:  global
        .offset:         48
        .size:           8
        .value_kind:     global_buffer
    .group_segment_fixed_size: 133120
    .kernarg_segment_align: 8
    .kernarg_segment_size: 56
    .language:       OpenCL C
    .language_version:
      - 2
      - 0
    .max_flat_workgroup_size: 768
    .name:           _Z8pam_mainPKDv4_jS1_S1_PKfS3_PDF16_Pf
    .private_segment_fixed_size: 0
    .sgpr_count:     52
    .sgpr_spill_count: 0
    .symbol:         _Z8pam_mainPKDv4_jS1_S1_PKfS3_PDF16_Pf.kd
    .uniform_work_group_size: 1
    .uses_dynamic_stack: false
    .vgpr_count:     152
    .vgpr_spill_count: 0
    .wavefront_size: 64
  - .agpr_count:     0
    .args:
      - .actual_access:  read_only
        .address_space:  global
        .offset:         0
        .size:           8
        .value_kind:     global_buffer
      - .actual_access:  read_only
        .address_space:  global
        .offset:         8
        .size:           8
        .value_kind:     global_buffer
      - .actual_access:  read_only
        .address_space:  global
        .offset:         16
        .size:           8
        .value_kind:     global_buffer
      - .actual_access:  read_only
        .address_space:  global
        .offset:         24
        .size:           8
        .value_kind:     global_buffer
      - .actual_access:  write_only
        .address_space:  global
        .offset:         32
        .size:           8
        .value_kind:     global_buffer
    .group_segment_fixed_size: 0
    .kernarg_segment_align: 8
    .kernarg_segment_size: 40
    .language:       OpenCL C
    .language_version:
      - 2
      - 0
    .max_flat_workgroup_size: 256
    .name:           _Z11pam_combinePKDF16_PKfS2_S2_Pf
    .private_segment_fixed_size: 0
    .sgpr_count:     38
    .sgpr_spill_count: 0
    .symbol:         _Z11pam_combinePKDF16_PKfS2_S2_Pf.kd
    .uniform_work_group_size: 1
    .uses_dynamic_stack: false
    .vgpr_count:     96
    .vgpr_spill_count: 0
    .wavefront_size: 64
